# speedup vs baseline: 1.0139x; 1.0139x over previous
_Z11init_kernelPKfS0_S0_S0_PDF16_S1_:
	s_load_dwordx2 s[6:7], s[0:1], 0x0
	s_load_dwordx2 s[8:9], s[0:1], 0x18
	s_lshl_b32 s4, s2, 4
	v_lshrrev_b32_e32 v14, 3, v0
	v_or_b32_e32 v2, s4, v14
	v_ashrrev_i32_e32 v3, 31, v2
	v_and_b32_e32 v1, 7, v0
	v_lshlrev_b64 v[12:13], 7, v[2:3]
	s_waitcnt lgkmcnt(0)
	v_lshl_add_u64 v[2:3], s[6:7], 0, v[12:13]
	v_mov_b32_e32 v11, 0
	v_lshlrev_b32_e32 v10, 4, v1
	v_lshl_add_u64 v[2:3], v[2:3], 0, v[10:11]
	global_load_dwordx4 v[32:35], v[2:3], off nt
	v_readfirstlane_b32 s11, v0
	v_cmp_gt_u32_e32 vcc, 16, v0
	s_and_saveexec_b64 s[2:3], vcc
	s_cbranch_execz .LBB0_2
	s_load_dwordx2 s[6:7], s[0:1], 0x8
	v_or_b32_e32 v2, s4, v0
	v_ashrrev_i32_e32 v3, 31, v2
	s_waitcnt lgkmcnt(0)
	v_lshl_add_u64 v[2:3], v[2:3], 4, s[6:7]
	global_load_dwordx4 v[36:39], v[2:3], off nt
.LBB0_2:
	s_or_b64 exec, exec, s[2:3]
	s_load_dwordx2 s[2:3], s[0:1], 0x10
	s_load_dwordx4 s[4:7], s[0:1], 0x20
	s_movk_i32 s10, 0x108
	v_mul_u32_u24_e32 v11, 0x108, v14
	v_mad_u32_u24 v40, v14, s10, v10
	v_mul_u32_u24_e32 v41, 0x108, v0
	s_mov_b64 s[12:13], vcc
	s_lshr_b32 s0, s11, 1
	v_mov_b32_e32 v3, 0
	s_and_b32 s0, s0, 0x7fffffe0
	v_and_b32_e32 v9, 15, v0
	v_or_b32_e32 v6, s0, v9
	v_mov_b32_e32 v7, v3
	v_lshl_add_u64 v[6:7], v[6:7], 2, s[8:9]
	v_bfe_u32 v8, v0, 4, 2
	global_load_dword a0, v[6:7], off
	v_lshlrev_b32_e32 v2, 8, v8
	s_mov_b32 s1, 0
	s_waitcnt lgkmcnt(0)
	v_lshl_add_u64 v[4:5], s[2:3], 0, v[2:3]
	v_lshl_add_u64 v[4:5], s[0:1], 2, v[4:5]
	v_lshlrev_b32_e32 v2, 2, v9
	v_lshl_add_u64 v[4:5], v[4:5], 0, v[2:3]
	global_load_dword v0, v[4:5], off
	global_load_dword a4, v[6:7], off offset:64
	global_load_dword v14, v[4:5], off offset:64
	global_load_dword v15, v[4:5], off offset:1024
	global_load_dword v16, v[4:5], off offset:1088
	global_load_dword v17, v[4:5], off offset:2048
	global_load_dword v18, v[4:5], off offset:2112
	global_load_dword v20, v[4:5], off offset:3072
	global_load_dword v21, v[4:5], off offset:3136
	s_movk_i32 s1, 0x1000
	v_lshlrev_b32_e32 v6, 2, v8
	v_mad_u32_u24 v19, v9, s10, v6
	v_add_co_u32_e32 v6, vcc, s1, v4
	s_movk_i32 s2, 0x2000
	s_nop 0
	v_addc_co_u32_e32 v7, vcc, 0, v5, vcc
	v_add_co_u32_e32 v4, vcc, s2, v4
	v_mul_u32_u24_e32 v8, 0x108, v8
	s_nop 0
	v_addc_co_u32_e32 v5, vcc, 0, v5, vcc
	global_load_dword v22, v[6:7], off offset:64
	global_load_dword v23, v[6:7], off offset:1024
	global_load_dword v24, v[6:7], off offset:1088
	global_load_dword v25, v[6:7], off offset:2048
	global_load_dword v26, v[6:7], off offset:2112
	global_load_dword v27, v[6:7], off offset:3072
	global_load_dword v28, v[6:7], off offset:3136
	global_load_dword v29, v[4:5], off offset:-4096
	global_load_dword v30, v[4:5], off
	global_load_dword v31, v[4:5], off offset:64
	s_waitcnt vmcnt(20)
	ds_write2_b64 v40, v[32:33], v[34:35] offset1:1
	s_and_saveexec_b64 s[14:15], s[12:13]
	ds_write2_b64 v41, v[36:37], v[38:39] offset0:16 offset1:17
	s_or_b64 exec, exec, s[14:15]
	s_waitcnt lgkmcnt(0)
	s_barrier
	ds_read2_b32 v[4:5], v19 offset1:4
	v_lshl_add_u64 v[6:7], s[6:7], 0, v[12:13]
	v_add_lshl_u32 v8, v8, s0, 2
	v_add_u32_e32 v2, v8, v2
	s_waitcnt vmcnt(19)
	v_accvgpr_mov_b32 a1, a0
	v_accvgpr_mov_b32 a2, a0
	v_accvgpr_mov_b32 a3, a0
	s_waitcnt vmcnt(17)
	v_accvgpr_mov_b32 a5, a4
	v_accvgpr_mov_b32 a6, a4
	v_accvgpr_mov_b32 a7, a4
	s_waitcnt lgkmcnt(0)
	v_mfma_f32_16x16x4_f32 a[0:3], v4, v0, a[0:3]
	s_waitcnt vmcnt(16)
	v_mfma_f32_16x16x4_f32 a[4:7], v4, v14, a[4:7]
	v_lshl_add_u32 v14, v1, 5, v11
	v_lshl_add_u64 v[0:1], s[4:5], 0, v[12:13]
	ds_read_b32 v12, v19 offset:128
	v_mul_u32_u24_e32 v13, 0x108, v9
	v_mul_i32_i24_e32 v9, 0xfffffefc, v9
	v_mov_b32_e32 v11, v3
	v_lshl_add_u64 v[0:1], v[0:1], 0, v[10:11]
	s_waitcnt vmcnt(15)
	v_mfma_f32_16x16x4_f32 a[0:3], v5, v15, a[0:3]
	v_lshl_add_u64 v[10:11], v[6:7], 0, v[10:11]
	v_add3_u32 v6, v13, v9, v8
	s_waitcnt vmcnt(14)
	v_mfma_f32_16x16x4_f32 a[4:7], v5, v16, a[4:7]
	ds_read2_b32 v[4:5], v19 offset0:8 offset1:12
	s_waitcnt vmcnt(13) lgkmcnt(0)
	v_mfma_f32_16x16x4_f32 a[0:3], v4, v17, a[0:3]
	s_waitcnt vmcnt(12)
	v_mfma_f32_16x16x4_f32 a[4:7], v4, v18, a[4:7]
	s_waitcnt vmcnt(11)
	v_mfma_f32_16x16x4_f32 a[0:3], v5, v20, a[0:3]
	s_waitcnt vmcnt(10)
	v_mfma_f32_16x16x4_f32 a[4:7], v5, v21, a[4:7]
	ds_read2_b32 v[4:5], v19 offset0:16 offset1:20
	s_waitcnt vmcnt(2) lgkmcnt(0)
	v_mfma_f32_16x16x4_f32 a[0:3], v4, v29, a[0:3]
	v_mfma_f32_16x16x4_f32 a[4:7], v4, v22, a[4:7]
	v_mfma_f32_16x16x4_f32 a[0:3], v5, v23, a[0:3]
	v_mfma_f32_16x16x4_f32 a[4:7], v5, v24, a[4:7]
	ds_read2_b32 v[4:5], v19 offset0:24 offset1:28
	s_waitcnt lgkmcnt(0)
	s_barrier
	v_mfma_f32_16x16x4_f32 a[0:3], v4, v25, a[0:3]
	v_mfma_f32_16x16x4_f32 a[4:7], v4, v26, a[4:7]
	v_mov_b32_e32 v4, v3
	v_mfma_f32_16x16x4_f32 a[0:3], v5, v27, a[0:3]
	v_mfma_f32_16x16x4_f32 a[4:7], v5, v28, a[4:7]
	v_mov_b32_e32 v5, v3
	s_waitcnt vmcnt(1)
	v_mfma_f32_16x16x4_f32 a[0:3], v12, v30, a[0:3]
	s_waitcnt vmcnt(0)
	v_mfma_f32_16x16x4_f32 a[4:7], v12, v31, a[4:7]
	s_nop 7
	ds_write_b32 v6, a0
	s_nop 0
	ds_write_b32 v2, a4 offset:64
	ds_write_b32 v6, a1 offset:264
	ds_write_b32 v2, a5 offset:328
	ds_write_b32 v6, a2 offset:528
	ds_write_b32 v2, a6 offset:592
	ds_write_b32 v6, a3 offset:792
	ds_write_b32 v2, a7 offset:856
	s_waitcnt lgkmcnt(0)
	s_barrier
	ds_read2_b32 v[6:7], v14 offset1:7
	ds_read2_b32 v[8:9], v14 offset0:1 offset1:2
	ds_read2_b32 v[12:13], v14 offset0:3 offset1:4
	ds_read2_b32 v[14:15], v14 offset0:5 offset1:6
	v_mov_b32_e32 v2, v3
	s_waitcnt lgkmcnt(3)
	v_cvt_f16_f32_e32 v6, v6
	s_waitcnt lgkmcnt(2)
	v_cvt_pk_f16_f32 v9, v8, v9
	s_waitcnt lgkmcnt(1)
	v_cvt_pk_f16_f32 v8, v12, v13
	v_cvt_f16_f32_e32 v13, v7
	s_waitcnt lgkmcnt(0)
	v_cvt_pk_f16_f32 v12, v14, v15
	v_alignbit_b32 v7, v8, v9, 16
	v_alignbit_b32 v8, v12, v8, 16
	v_pack_b32_f16 v6, v6, v9
	v_alignbit_b32 v9, v13, v12, 16
	global_store_dwordx4 v[0:1], v[6:9], off
	global_store_dwordx4 v[10:11], v[2:5], off
	s_endpgm
	.p2align	8

	.amdhsa_kernel _Z11init_kernelPKfS0_S0_S0_PDF16_S1_
		.amdhsa_group_segment_fixed_size 4224
		.amdhsa_private_segment_fixed_size 0
		.amdhsa_kernarg_size 48
		.amdhsa_user_sgpr_count 2
		.amdhsa_user_sgpr_dispatch_ptr 0
		.amdhsa_user_sgpr_queue_ptr 0
		.amdhsa_user_sgpr_kernarg_segment_ptr 1
		.amdhsa_user_sgpr_dispatch_id 0
		.amdhsa_user_sgpr_kernarg_preload_length 0
		.amdhsa_user_sgpr_kernarg_preload_offset 0
		.amdhsa_user_sgpr_private_segment_size 0
		.amdhsa_uses_dynamic_stack 0
		.amdhsa_enable_private_segment 0
		.amdhsa_system_sgpr_workgroup_id_x 1
		.amdhsa_system_sgpr_workgroup_id_y 0
		.amdhsa_system_sgpr_workgroup_id_z 0
		.amdhsa_system_sgpr_workgroup_info 0
		.amdhsa_system_vgpr_workitem_id 0
		.amdhsa_next_free_vgpr 52
		.amdhsa_next_free_sgpr 16
		.amdhsa_accum_offset 44
		.amdhsa_reserve_vcc 1
		.amdhsa_float_round_mode_32 0
		.amdhsa_float_round_mode_16_64 0
		.amdhsa_float_denorm_mode_32 3
		.amdhsa_float_denorm_mode_16_64 3
		.amdhsa_dx10_clamp 1
		.amdhsa_ieee_mode 1
		.amdhsa_fp16_overflow 0
		.amdhsa_tg_split 0
		.amdhsa_exception_fp_ieee_invalid_op 0
		.amdhsa_exception_fp_denorm_src 0
		.amdhsa_exception_fp_ieee_div_zero 0
		.amdhsa_exception_fp_ieee_overflow 0
		.amdhsa_exception_fp_ieee_underflow 0
		.amdhsa_exception_fp_ieee_inexact 0
		.amdhsa_exception_int_div_zero 0
	.end_amdhsa_kernel

_Z12final_kernelPKDF16_S0_PKfS2_S2_S2_Pf:
	s_load_dwordx8 s[4:11], s[0:1], 0x0
	s_load_dwordx2 s[14:15], s[0:1], 0x20
	s_load_dwordx4 s[16:19], s[0:1], 0x28
	s_lshl_b32 s12, s2, 4
	v_lshrrev_b32_e32 v1, 3, v0
	v_or_b32_e32 v2, s12, v1
	v_ashrrev_i32_e32 v3, 31, v2
	v_and_b32_e32 v20, 7, v0
	v_lshlrev_b64 v[2:3], 7, v[2:3]
	v_lshrrev_b32_e32 v50, 6, v0
	v_and_b32_e32 v51, 15, v0
	v_lshlrev_b32_e32 v50, 7, v50
	v_lshl_or_b32 v51, v51, 2, v50
	s_waitcnt lgkmcnt(0)
	s_load_dword s13, s[16:17], 0x0
	global_load_dword v50, v51, s[14:15]
	global_load_dword v51, v51, s[14:15] offset:64
	v_lshl_add_u64 v[2:3], s[4:5], 0, v[2:3]
	v_lshlrev_b32_e32 v6, 4, v20
	v_mov_b32_e32 v7, 0
	v_lshl_add_u64 v[2:3], v[2:3], 0, v[6:7]
	global_load_dwordx4 v[2:5], v[2:3], off nt
	v_readfirstlane_b32 s4, v0
	v_bfe_u32 v21, v0, 4, 2
	s_lshr_b32 s2, s4, 1
	v_lshlrev_b32_e32 v6, 8, v21
	s_mov_b32 s3, 0
	v_and_b32_e32 v22, 15, v0
	s_and_b32 s2, s2, 0x7fffffe0
	v_lshl_add_u64 v[16:17], s[8:9], 0, v[6:7]
	v_lshlrev_b32_e32 v23, 2, v21
	s_andn2_b32 s4, s4, 63
	v_lshlrev_b32_e32 v6, 2, v22
	v_lshl_add_u64 v[16:17], s[2:3], 2, v[16:17]
	v_or_b32_e32 v8, s12, v23
	s_add_u32 s6, s6, s4
	v_lshl_add_u64 v[16:17], v[16:17], 0, v[6:7]
	v_or_b32_e32 v6, s2, v22
	v_ashrrev_i32_e32 v9, 31, v8
	v_or_b32_e32 v10, 1, v8
	s_addc_u32 s7, s7, 0
	v_lshlrev_b64 v[18:19], 2, v[6:7]
	v_lshlrev_b32_e32 v6, 1, v22
	v_lshlrev_b64 v[14:15], 7, v[8:9]
	v_ashrrev_i32_e32 v11, 31, v10
	v_lshl_add_u64 v[6:7], s[6:7], 0, v[6:7]
	v_lshlrev_b64 v[10:11], 7, v[10:11]
	v_lshl_add_u64 v[14:15], v[6:7], 0, v[14:15]
	v_lshl_add_u64 v[10:11], v[6:7], 0, v[10:11]
	global_load_ushort v24, v[14:15], off nt
	global_load_ushort v25, v[14:15], off offset:32 nt
	global_load_ushort v26, v[10:11], off nt
	v_lshl_add_u64 v[14:15], s[10:11], 0, v[18:19]
	v_or_b32_e32 v12, 2, v8
	v_or_b32_e32 v8, 3, v8
	global_load_dword v27, v[14:15], off
	global_load_dword v28, v[14:15], off offset:64
	v_ashrrev_i32_e32 v13, 31, v12
	v_ashrrev_i32_e32 v9, 31, v8
	v_lshlrev_b64 v[12:13], 7, v[12:13]
	v_lshlrev_b64 v[8:9], 7, v[8:9]
	v_lshl_add_u64 v[12:13], v[6:7], 0, v[12:13]
	v_lshl_add_u64 v[6:7], v[6:7], 0, v[8:9]
	global_load_ushort v14, v[10:11], off offset:32 nt
	global_load_ushort v15, v[12:13], off nt
	global_load_ushort v29, v[6:7], off nt
	v_lshlrev_b32_e32 v8, 5, v20
	global_load_ushort v10, v[12:13], off offset:32 nt
	global_load_ushort v11, v[6:7], off offset:32 nt
	global_load_dword v20, v[16:17], off
	global_load_dword v30, v[16:17], off offset:64
	global_load_dword v31, v[16:17], off offset:1024
	global_load_dword v32, v[16:17], off offset:1088
	global_load_dword v33, v[16:17], off offset:2048
	global_load_dword v34, v[16:17], off offset:2112
	global_load_dword v35, v[16:17], off offset:3072
	global_load_dword v36, v[16:17], off offset:3136
	s_movk_i32 s2, 0x108
	v_mad_u32_u24 v1, v1, s2, v8
	s_movk_i32 s3, 0x1000
	v_mad_u32_u24 v23, v22, s2, v23
	s_addk_i32 s4, 0x1080
	s_waitcnt vmcnt(18)
	v_cvt_f32_f16_e32 v6, v2
	v_cvt_f32_f16_sdwa v7, v2 dst_sel:DWORD dst_unused:UNUSED_PAD src0_sel:WORD_1
	v_cvt_f32_f16_e32 v8, v3
	v_cvt_f32_f16_sdwa v9, v3 dst_sel:DWORD dst_unused:UNUSED_PAD src0_sel:WORD_1
	v_cvt_f32_f16_e32 v12, v4
	v_cvt_f32_f16_sdwa v13, v4 dst_sel:DWORD dst_unused:UNUSED_PAD src0_sel:WORD_1
	v_cvt_f32_f16_e32 v37, v5
	v_cvt_f32_f16_sdwa v38, v5 dst_sel:DWORD dst_unused:UNUSED_PAD src0_sel:WORD_1
	v_max_f32_e32 v2, 0, v6
	v_max_f32_e32 v3, 0, v7
	v_max_f32_e32 v4, 0, v8
	v_max_f32_e32 v5, 0, v9
	v_max_f32_e32 v6, 0, v12
	v_max_f32_e32 v7, 0, v13
	v_max_f32_e32 v8, 0, v37
	v_max_f32_e32 v9, 0, v38
	ds_write2_b64 v1, v[2:3], v[4:5] offset1:1
	ds_write2_b64 v1, v[6:7], v[8:9] offset0:2 offset1:3
	v_add_co_u32_e32 v2, vcc, s3, v16
	s_movk_i32 s3, 0x2000
	s_nop 0
	v_addc_co_u32_e32 v3, vcc, 0, v17, vcc
	v_add_co_u32_e32 v4, vcc, s3, v16
	s_movk_i32 s3, 0x3000
	s_nop 0
	v_addc_co_u32_e32 v5, vcc, 0, v17, vcc
	global_load_dword v1, v[4:5], off offset:-4096
	global_load_dword v6, v[4:5], off
	global_load_dword v7, v[4:5], off offset:64
	global_load_dword v8, v[4:5], off offset:1024
	global_load_dword v9, v[4:5], off offset:1088
	global_load_dword v12, v[4:5], off offset:2048
	global_load_dword v13, v[4:5], off offset:2112
	global_load_dword v37, v[4:5], off offset:3072
	global_load_dword v38, v[4:5], off offset:3136
	v_add_co_u32_e32 v4, vcc, s3, v16
	s_nop 1
	v_addc_co_u32_e32 v5, vcc, 0, v17, vcc
	global_load_dword v16, v[2:3], off offset:64
	global_load_dword v17, v[2:3], off offset:1024
	global_load_dword v39, v[2:3], off offset:1088
	global_load_dword v40, v[2:3], off offset:2048
	global_load_dword v41, v[2:3], off offset:2112
	global_load_dword v42, v[2:3], off offset:3072
	global_load_dword v43, v[2:3], off offset:3136
	global_load_dword v44, v[4:5], off
	s_waitcnt vmcnt(34)
	v_cvt_f32_f16_e32 v2, v24
	s_waitcnt vmcnt(33)
	v_cvt_f32_f16_e32 v3, v25
	s_waitcnt vmcnt(32)
	v_cvt_f32_f16_e32 v24, v26
	global_load_dword v25, v[4:5], off offset:64
	global_load_dword v26, v[4:5], off offset:1024
	global_load_dword v45, v[4:5], off offset:1088
	global_load_dword v46, v[4:5], off offset:2048
	global_load_dword v47, v[4:5], off offset:2112
	global_load_dword v48, v[4:5], off offset:3072
	global_load_dword v49, v[4:5], off offset:3136
	s_waitcnt vmcnt(38)
	v_add_f32_e32 v4, v27, v2
	s_waitcnt vmcnt(37)
	v_add_f32_e32 v5, v28, v3
	s_waitcnt lgkmcnt(0)
	s_barrier
	ds_read2_b32 v[2:3], v23 offset1:4
	s_waitcnt vmcnt(36)
	v_cvt_f32_f16_e32 v14, v14
	s_waitcnt vmcnt(35)
	v_cvt_f32_f16_e32 v15, v15
	s_waitcnt vmcnt(34)
	v_cvt_f32_f16_e32 v29, v29
	s_waitcnt vmcnt(33)
	v_cvt_f32_f16_e32 v10, v10
	s_waitcnt vmcnt(32)
	v_cvt_f32_f16_e32 v11, v11
	v_add_f32_e32 v24, v27, v24
	v_add_f32_e32 v15, v27, v15
	v_add_f32_e32 v27, v27, v29
	v_accvgpr_write_b32 a0, v4
	v_add_f32_e32 v4, v28, v14
	v_add_f32_e32 v10, v28, v10
	v_add_f32_e32 v11, v28, v11
	v_accvgpr_write_b32 a1, v24
	v_accvgpr_write_b32 a2, v15
	v_accvgpr_write_b32 a3, v27
	v_accvgpr_write_b32 a4, v5
	v_accvgpr_write_b32 a5, v4
	v_accvgpr_write_b32 a6, v10
	v_accvgpr_write_b32 a7, v11
	s_waitcnt vmcnt(31) lgkmcnt(0)
	v_mfma_f32_16x16x4_f32 a[0:3], v2, v20, a[0:3]
	s_waitcnt vmcnt(30)
	v_mfma_f32_16x16x4_f32 a[4:7], v2, v30, a[4:7]
	s_waitcnt vmcnt(29)
	v_mfma_f32_16x16x4_f32 a[0:3], v3, v31, a[0:3]
	s_waitcnt vmcnt(28)
	v_mfma_f32_16x16x4_f32 a[4:7], v3, v32, a[4:7]
	ds_read2_b32 v[2:3], v23 offset0:8 offset1:12
	s_waitcnt vmcnt(27) lgkmcnt(0)
	v_mfma_f32_16x16x4_f32 a[0:3], v2, v33, a[0:3]
	s_waitcnt vmcnt(26)
	v_mfma_f32_16x16x4_f32 a[4:7], v2, v34, a[4:7]
	s_waitcnt vmcnt(25)
	v_mfma_f32_16x16x4_f32 a[0:3], v3, v35, a[0:3]
	s_waitcnt vmcnt(24)
	v_mfma_f32_16x16x4_f32 a[4:7], v3, v36, a[4:7]
	ds_read2_b32 v[2:3], v23 offset0:16 offset1:20
	s_waitcnt vmcnt(23) lgkmcnt(0)
	v_mfma_f32_16x16x4_f32 a[0:3], v2, v1, a[0:3]
	s_waitcnt vmcnt(14)
	v_mfma_f32_16x16x4_f32 a[4:7], v2, v16, a[4:7]
	s_waitcnt vmcnt(13)
	v_mfma_f32_16x16x4_f32 a[0:3], v3, v17, a[0:3]
	s_waitcnt vmcnt(12)
	v_mfma_f32_16x16x4_f32 a[4:7], v3, v39, a[4:7]
	ds_read2_b32 v[2:3], v23 offset0:24 offset1:28
	s_waitcnt vmcnt(11) lgkmcnt(0)
	v_mfma_f32_16x16x4_f32 a[0:3], v2, v40, a[0:3]
	s_waitcnt vmcnt(10)
	v_mfma_f32_16x16x4_f32 a[4:7], v2, v41, a[4:7]
	s_waitcnt vmcnt(9)
	v_mfma_f32_16x16x4_f32 a[0:3], v3, v42, a[0:3]
	s_waitcnt vmcnt(8)
	v_mfma_f32_16x16x4_f32 a[4:7], v3, v43, a[4:7]
	ds_read2_b32 v[2:3], v23 offset0:32 offset1:36
	s_waitcnt lgkmcnt(0)
	v_mfma_f32_16x16x4_f32 a[0:3], v2, v6, a[0:3]
	v_mfma_f32_16x16x4_f32 a[4:7], v2, v7, a[4:7]
	ds_read2_b32 v[6:7], v23 offset0:56 offset1:60
	v_mfma_f32_16x16x4_f32 a[0:3], v3, v8, a[0:3]
	v_mfma_f32_16x16x4_f32 a[4:7], v3, v9, a[4:7]
	ds_read2_b32 v[2:3], v23 offset0:40 offset1:44
	s_waitcnt lgkmcnt(0)
	v_mfma_f32_16x16x4_f32 a[0:3], v2, v12, a[0:3]
	v_mfma_f32_16x16x4_f32 a[4:7], v2, v13, a[4:7]
	v_mfma_f32_16x16x4_f32 a[0:3], v3, v37, a[0:3]
	v_mfma_f32_16x16x4_f32 a[4:7], v3, v38, a[4:7]
	ds_read2_b32 v[2:3], v23 offset0:48 offset1:52
	s_waitcnt vmcnt(7) lgkmcnt(0)
	v_mfma_f32_16x16x4_f32 a[0:3], v2, v44, a[0:3]
	s_waitcnt vmcnt(6)
	v_mfma_f32_16x16x4_f32 a[4:7], v2, v25, a[4:7]
	s_waitcnt vmcnt(5)
	v_mfma_f32_16x16x4_f32 a[0:3], v3, v26, a[0:3]
	s_waitcnt vmcnt(4)
	v_mfma_f32_16x16x4_f32 a[4:7], v3, v45, a[4:7]
	s_waitcnt vmcnt(3)
	v_mfma_f32_16x16x4_f32 a[0:3], v6, v46, a[0:3]
	s_waitcnt vmcnt(1)
	v_mfma_f32_16x16x4_f32 a[0:3], v7, v48, a[0:3]
	v_mfma_f32_16x16x4_f32 a[4:7], v6, v47, a[4:7]
	s_waitcnt vmcnt(0)
	v_mfma_f32_16x16x4_f32 a[4:7], v7, v49, a[4:7]
	v_lshlrev_b32_e32 v12, 4, v21
	v_cmp_eq_u32_e32 vcc, 0, v22
	v_add_u32_e32 v12, s4, v12
	s_nop 9
	v_accvgpr_read_b32 v2, a0
	v_accvgpr_read_b32 v3, a1
	v_accvgpr_read_b32 v4, a2
	v_accvgpr_read_b32 v5, a3
	v_accvgpr_read_b32 v6, a4
	v_accvgpr_read_b32 v7, a5
	v_accvgpr_read_b32 v8, a6
	v_accvgpr_read_b32 v9, a7
	v_max_f32_e32 v2, 0, v2
	v_max_f32_e32 v3, 0, v3
	v_max_f32_e32 v4, 0, v4
	v_max_f32_e32 v5, 0, v5
	v_max_f32_e32 v6, 0, v6
	v_max_f32_e32 v7, 0, v7
	v_max_f32_e32 v8, 0, v8
	v_max_f32_e32 v9, 0, v9
	v_mul_f32_e32 v6, v51, v6
	v_mul_f32_e32 v7, v51, v7
	v_mul_f32_e32 v8, v51, v8
	v_mul_f32_e32 v9, v51, v9
	v_fmac_f32_e32 v6, v50, v2
	v_fmac_f32_e32 v7, v50, v3
	v_fmac_f32_e32 v8, v50, v4
	v_fmac_f32_e32 v9, v50, v5
	v_add_f32_dpp v6, v6, v6 quad_perm:[1,0,3,2] row_mask:0xf bank_mask:0xf
	v_add_f32_dpp v7, v7, v7 quad_perm:[1,0,3,2] row_mask:0xf bank_mask:0xf
	v_add_f32_dpp v8, v8, v8 quad_perm:[1,0,3,2] row_mask:0xf bank_mask:0xf
	v_add_f32_dpp v9, v9, v9 quad_perm:[1,0,3,2] row_mask:0xf bank_mask:0xf
	v_add_f32_dpp v6, v6, v6 quad_perm:[2,3,0,1] row_mask:0xf bank_mask:0xf
	v_add_f32_dpp v7, v7, v7 quad_perm:[2,3,0,1] row_mask:0xf bank_mask:0xf
	v_add_f32_dpp v8, v8, v8 quad_perm:[2,3,0,1] row_mask:0xf bank_mask:0xf
	v_add_f32_dpp v9, v9, v9 quad_perm:[2,3,0,1] row_mask:0xf bank_mask:0xf
	v_add_f32_dpp v6, v6, v6 row_half_mirror row_mask:0xf bank_mask:0xf
	v_add_f32_dpp v7, v7, v7 row_half_mirror row_mask:0xf bank_mask:0xf
	v_add_f32_dpp v8, v8, v8 row_half_mirror row_mask:0xf bank_mask:0xf
	v_add_f32_dpp v9, v9, v9 row_half_mirror row_mask:0xf bank_mask:0xf
	v_add_f32_dpp v6, v6, v6 row_mirror row_mask:0xf bank_mask:0xf
	v_add_f32_dpp v7, v7, v7 row_mirror row_mask:0xf bank_mask:0xf
	v_add_f32_dpp v8, v8, v8 row_mirror row_mask:0xf bank_mask:0xf
	v_add_f32_dpp v9, v9, v9 row_mirror row_mask:0xf bank_mask:0xf
	s_and_saveexec_b64 s[2:3], vcc
	ds_write_b128 v12, v[6:9]
	s_or_b64 exec, exec, s[2:3]
	v_cmp_gt_u32_e32 vcc, 16, v0
	s_waitcnt lgkmcnt(0)
	s_barrier
	s_and_saveexec_b64 s[2:3], vcc
	s_cbranch_execz .LBB1_10
	v_lshlrev_b32_e32 v1, 2, v0
	v_add_u32_e32 v1, 0x1000, v1
	ds_read2_b32 v[2:3], v1 offset0:32 offset1:48
	v_or_b32_e32 v0, s12, v0
	v_ashrrev_i32_e32 v1, 31, v0
	v_lshl_add_u64 v[0:1], v[0:1], 2, s[18:19]
	s_waitcnt lgkmcnt(0)
	v_add_f32_e32 v2, v2, v3
	v_add_f32_e32 v2, s13, v2
	global_store_dword v[0:1], v2, off

	.amdhsa_kernel _Z12final_kernelPKDF16_S0_PKfS2_S2_S2_Pf
		.amdhsa_group_segment_fixed_size 4352
		.amdhsa_private_segment_fixed_size 0
		.amdhsa_kernarg_size 56
		.amdhsa_user_sgpr_count 2
		.amdhsa_user_sgpr_dispatch_ptr 0
		.amdhsa_user_sgpr_queue_ptr 0
		.amdhsa_user_sgpr_kernarg_segment_ptr 1
		.amdhsa_user_sgpr_dispatch_id 0
		.amdhsa_user_sgpr_kernarg_preload_length 0
		.amdhsa_user_sgpr_kernarg_preload_offset 0
		.amdhsa_user_sgpr_private_segment_size 0
		.amdhsa_uses_dynamic_stack 0
		.amdhsa_enable_private_segment 0
		.amdhsa_system_sgpr_workgroup_id_x 1
		.amdhsa_system_sgpr_workgroup_id_y 0
		.amdhsa_system_sgpr_workgroup_id_z 0
		.amdhsa_system_sgpr_workgroup_info 0
		.amdhsa_system_vgpr_workitem_id 0
		.amdhsa_next_free_vgpr 60
		.amdhsa_next_free_sgpr 20
		.amdhsa_accum_offset 52
		.amdhsa_reserve_vcc 1
		.amdhsa_float_round_mode_32 0
		.amdhsa_float_round_mode_16_64 0
		.amdhsa_float_denorm_mode_32 3
		.amdhsa_float_denorm_mode_16_64 3
		.amdhsa_dx10_clamp 1
		.amdhsa_ieee_mode 1
		.amdhsa_fp16_overflow 0
		.amdhsa_tg_split 0
		.amdhsa_exception_fp_ieee_invalid_op 0
		.amdhsa_exception_fp_denorm_src 0
		.amdhsa_exception_fp_ieee_div_zero 0
		.amdhsa_exception_fp_ieee_overflow 0
		.amdhsa_exception_fp_ieee_underflow 0
		.amdhsa_exception_fp_ieee_inexact 0
		.amdhsa_exception_int_div_zero 0
	.end_amdhsa_kernel

amdhsa.kernels:
  - .agpr_count:     8
    .args:
      - .actual_access:  read_only
        .address_space:  global
        .offset:         0
        .size:           8
        .value_kind:     global_buffer
      - .actual_access:  read_only
        .address_space:  global
        .offset:         8
        .size:           8
        .value_kind:     global_buffer
      - .actual_access:  read_only
        .address_space:  global
        .offset:         16
        .size:           8
        .value_kind:     global_buffer
      - .actual_access:  read_only
        .address_space:  global
        .offset:         24
        .size:           8
        .value_kind:     global_buffer
      - .actual_access:  write_only
        .address_space:  global
        .offset:         32
        .size:           8
        .value_kind:     global_buffer
      - .actual_access:  write_only
        .address_space:  global
        .offset:         40
        .size:           8
        .value_kind:     global_buffer
    .group_segment_fixed_size: 4224
    .kernarg_segment_align: 8
    .kernarg_segment_size: 48
    .language:       OpenCL C
    .language_version:
      - 2
      - 0
    .max_flat_workgroup_size: 128
    .name:           _Z11init_kernelPKfS0_S0_S0_PDF16_S1_
    .private_segment_fixed_size: 0
    .sgpr_count:     22
    .sgpr_spill_count: 0
    .symbol:         _Z11init_kernelPKfS0_S0_S0_PDF16_S1_.kd
    .uniform_work_group_size: 1
    .uses_dynamic_stack: false
    .vgpr_count:     52
    .vgpr_spill_count: 0
    .wavefront_size: 64
  - .agpr_count:     8
    .args:
      - .actual_access:  read_only
        .address_space:  global
        .offset:         0
        .size:           8
        .value_kind:     global_buffer
      - .actual_access:  read_only
        .address_space:  global
        .offset:         8
        .size:           8
        .value_kind:     global_buffer
      - .actual_access:  read_only
        .address_space:  global
        .offset:         16
        .size:           8
        .value_kind:     global_buffer
      - .actual_access:  read_only
        .address_space:  global
        .offset:         24
        .size:           8
        .value_kind:     global_buffer
      - .actual_access:  read_only
        .address_space:  global
        .offset:         32
        .size:           8
        .value_kind:     global_buffer
      - .actual_access:  read_only
        .address_space:  global
        .offset:         40
        .size:           8
        .value_kind:     global_buffer
      - .actual_access:  write_only
        .address_space:  global
        .offset:         48
        .size:           8
        .value_kind:     global_buffer
    .group_segment_fixed_size: 4352
    .kernarg_segment_align: 8
    .kernarg_segment_size: 56
    .language:       OpenCL C
    .language_version:
      - 2
      - 0
    .max_flat_workgroup_size: 128
    .name:           _Z12final_kernelPKDF16_S0_PKfS2_S2_S2_Pf
    .private_segment_fixed_size: 0
    .sgpr_count:     26
    .sgpr_spill_count: 0
    .symbol:         _Z12final_kernelPKDF16_S0_PKfS2_S2_S2_Pf.kd
    .uniform_work_group_size: 1
    .uses_dynamic_stack: false
    .vgpr_count:     60
    .vgpr_spill_count: 0
    .wavefront_size: 64
  - .agpr_count:     0
    .args:
      - .actual_access:  read_only
        .address_space:  global
        .offset:         0
        .size:           8
        .value_kind:     global_buffer
      - .actual_access:  read_only
        .address_space:  global
        .offset:         8
        .size:           8
        .value_kind:     global_buffer
      - .actual_access:  read_only
        .address_space:  global
        .offset:         16
        .size:           8
        .value_kind:     global_buffer
      - .actual_access:  read_only
        .address_space:  global
        .offset:         24
        .size:           8
        .value_kind:     global_buffer
      - .actual_access:  read_only
        .address_space:  global
        .offset:         32
        .size:           8
        .value_kind:     global_buffer
      - .actual_access:  read_only
        .address_space:  global
        .offset:         40
        .size:           8
        .value_kind:     global_buffer
      - .actual_access:  read_only
        .address_space:  global
        .offset:         48
        .size:           8
        .value_kind:     global_buffer
      - .actual_access:  read_only
        .address_space:  global
        .offset:         56
        .size:           8
        .value_kind:     global_buffer
      - .actual_access:  read_only
        .address_space:  global
        .offset:         64
        .size:           8
        .value_kind:     global_buffer
      - .actual_access:  read_only
        .address_space:  global
        .offset:         72
        .size:           8
        .value_kind:     global_buffer
      - .address_space:  global
        .offset:         80
        .size:           8
        .value_kind:     global_buffer
    .group_segment_fixed_size: 16896
    .kernarg_segment_align: 8
    .kernarg_segment_size: 88
    .language:       OpenCL C
    .language_version:
      - 2
      - 0
    .max_flat_workgroup_size: 128
    .name:           _Z11edge_kernelILi36ELb1EEvPKfS1_PKDF16_PKiS5_S1_S1_S1_S1_S1_PDF16_
    .private_segment_fixed_size: 0
    .sgpr_count:     23
    .sgpr_spill_count: 0
    .symbol:         _Z11edge_kernelILi36ELb1EEvPKfS1_PKDF16_PKiS5_S1_S1_S1_S1_S1_PDF16_.kd
    .uniform_work_group_size: 1
    .uses_dynamic_stack: false
    .vgpr_count:     138
    .vgpr_spill_count: 0
    .wavefront_size: 64
  - .agpr_count:     0
    .args:
      - .actual_access:  read_only
        .address_space:  global
        .offset:         0
        .size:           8
        .value_kind:     global_buffer
      - .actual_access:  read_only
        .address_space:  global
        .offset:         8
        .size:           8
        .value_kind:     global_buffer
      - .actual_access:  read_only
        .address_space:  global
        .offset:         16
        .size:           8
        .value_kind:     global_buffer
      - .actual_access:  read_only
        .address_space:  global
        .offset:         24
        .size:           8
        .value_kind:     global_buffer
      - .actual_access:  read_only
        .address_space:  global
        .offset:         32
        .size:           8
        .value_kind:     global_buffer
      - .actual_access:  read_only
        .address_space:  global
        .offset:         40
        .size:           8
        .value_kind:     global_buffer
      - .actual_access:  read_only
        .address_space:  global
        .offset:         48
        .size:           8
        .value_kind:     global_buffer
      - .actual_access:  read_only
        .address_space:  global
        .offset:         56
        .size:           8
        .value_kind:     global_buffer
      - .actual_access:  read_only
        .address_space:  global
        .offset:         64
        .size:           8
        .value_kind:     global_buffer
      - .actual_access:  read_only
        .address_space:  global
        .offset:         72
        .size:           8
        .value_kind:     global_buffer
      - .address_space:  global
        .offset:         80
        .size:           8
        .value_kind:     global_buffer
    .group_segment_fixed_size: 16896
    .kernarg_segment_align: 8
    .kernarg_segment_size: 88
    .language:       OpenCL C
    .language_version:
      - 2
      - 0
    .max_flat_workgroup_size: 128
    .name:           _Z11edge_kernelILi64ELb0EEvPKfS1_PKDF16_PKiS5_S1_S1_S1_S1_S1_PDF16_
    .private_segment_fixed_size: 0
    .sgpr_count:     26
    .sgpr_spill_count: 0
    .symbol:         _Z11edge_kernelILi64ELb0EEvPKfS1_PKDF16_PKiS5_S1_S1_S1_S1_S1_PDF16_.kd
    .uniform_work_group_size: 1
    .uses_dynamic_stack: false
    .vgpr_count:     166
    .vgpr_spill_count: 0
    .wavefront_size: 64
